# speedup vs baseline: 1.0505x; 1.0505x over previous
.Lcmb_m1:
	v_fmac_f32_e32 v56, s17, v48
	v_fmac_f32_e32 v57, s17, v49
	v_fmac_f32_e32 v58, s17, v50
	v_fmac_f32_e32 v59, s17, v51
	v_fmac_f32_e32 v60, s17, v52
	v_fmac_f32_e32 v61, s17, v53
	v_fmac_f32_e32 v62, s17, v54
	v_fmac_f32_e32 v63, s17, v55
	global_store_dwordx4 v3, v[56:59], s[10:11] nt
	global_store_dwordx4 v3, v[60:63], s[10:11] offset:16 nt
	s_endpgm
	.p2align	8
